# LN2 (layer 0): the next token's residual row is requested right after the current token's values are converted (prefetch one token ahead; vmcnt ladder accounts for the 16 stores in between)
# baseline (speedup 1.0000x reference)
; #define LAS __attribute__((address_space(3)))
; __device__ __forceinline__ void peer_ln2_phase(LAS unsigned char* lds, int wave, int blk, const bf16* __restrict__ X1B, const bf16* __restrict__ YT, const float* __restrict__ g2, const float* __restrict__ b2, ...
;     ...
;     float gv[16], bv[16];
; #pragma unroll
;     for (int k = 0; k < 16; ++k) { gv[k] = g2[lane + 64 * k]; bv[k] = b2[lane + 64 * k]; }
; #pragma unroll 1
;     for (int i = 0; i < 8; ++i) {
;         const int tk = wave * 8 + i; const size_t t = (size_t)blk * 64 + tk;
;         float z[16]; float s = 0.f;
; #pragma unroll
;         for (int k = 0; k < 16; ++k) { const float xv = __uint_as_float((unsigned)__builtin_nontemporal_load((const unsigned short*)X1B + t * 1024 + lane + 64 * k) << 16); const unsigned yb = *(const LAS unsigned short*)(lds + (lane + 64 * k) * 136 + tk * 2);
;             z[k] = 1.41421356237309515f * xv + __uint_as_float(yb << 16); s += z[k]; }
.LBB0_1025:
	s_or_b64 exec, exec, s[12:13]
	v_ashrrev_i32_e32 v1, 31, v0
	v_lshlrev_b64 v[2:3], 2, v[0:1]
	v_lshl_add_u64 v[36:37], s[4:5], 0, v[2:3]
	s_waitcnt lgkmcnt(0)
	s_barrier
	v_lshl_add_u64 v[2:3], s[6:7], 0, v[2:3]
	global_load_dword v4, v[36:37], off
	global_load_dword v5, v[36:37], off offset:256
	global_load_dword v6, v[36:37], off offset:512
	global_load_dword v7, v[36:37], off offset:768
	global_load_dword v9, v[36:37], off offset:1024
	global_load_dword v10, v[36:37], off offset:1280
	global_load_dword v11, v[36:37], off offset:1536
	global_load_dword v12, v[36:37], off offset:1792
	global_load_dword v13, v[2:3], off
	global_load_dword v14, v[2:3], off offset:256
	global_load_dword v15, v[2:3], off offset:512
	global_load_dword v16, v[2:3], off offset:768
	global_load_dword v17, v[2:3], off offset:1024
	global_load_dword v18, v[2:3], off offset:1280
	global_load_dword v19, v[2:3], off offset:1536
	global_load_dword v20, v[2:3], off offset:1792
	global_load_dword v21, v[36:37], off offset:2048
	global_load_dword v22, v[36:37], off offset:2304
	global_load_dword v23, v[36:37], off offset:2560
	global_load_dword v24, v[36:37], off offset:2816
	global_load_dword v25, v[36:37], off offset:3072
	global_load_dword v26, v[36:37], off offset:3328
	global_load_dword v27, v[36:37], off offset:3584
	global_load_dword v28, v[36:37], off offset:3840
	global_load_dword v29, v[2:3], off offset:2048
	global_load_dword v30, v[2:3], off offset:2304
	global_load_dword v31, v[2:3], off offset:2560
	global_load_dword v32, v[2:3], off offset:2816
	global_load_dword v33, v[2:3], off offset:3072
	global_load_dword v34, v[2:3], off offset:3328
	global_load_dword v35, v[2:3], off offset:3584
	global_load_dword v36, v[2:3], off offset:3840
	v_and_b32_e32 v2, 64, v8
	v_add_u32_e32 v2, 64, v2
	v_xor_b32_e32 v3, 1, v8
	v_cmp_lt_i32_e32 vcc, v3, v2
	s_movk_i32 s5, 0x88
	s_lshl_b32 s4, s61, 3
	v_cndmask_b32_e32 v3, v8, v3, vcc
	v_lshlrev_b32_e32 v37, 2, v3
	v_xor_b32_e32 v3, 2, v8
	v_cmp_lt_i32_e32 vcc, v3, v2
	s_mov_b64 s[6:7], 0
	v_mov_b32_e32 v44, 0x3727c5ac
	v_cndmask_b32_e32 v3, v8, v3, vcc
	v_lshlrev_b32_e32 v38, 2, v3
	v_xor_b32_e32 v3, 4, v8
	v_cmp_lt_i32_e32 vcc, v3, v2
	v_mov_b32_e32 v45, 0x260
	s_nop 0
	v_cndmask_b32_e32 v3, v8, v3, vcc
	v_lshlrev_b32_e32 v39, 2, v3
	v_xor_b32_e32 v3, 8, v8
	v_cmp_lt_i32_e32 vcc, v3, v2
	s_nop 1
	v_cndmask_b32_e32 v3, v8, v3, vcc
	v_lshlrev_b32_e32 v40, 2, v3
	v_xor_b32_e32 v3, 16, v8
	v_cmp_lt_i32_e32 vcc, v3, v2
	s_nop 1
	v_cndmask_b32_e32 v3, v8, v3, vcc
	v_lshlrev_b32_e32 v41, 2, v3
	v_xor_b32_e32 v3, 32, v8
	v_cmp_lt_i32_e32 vcc, v3, v2
	s_nop 1
	v_cndmask_b32_e32 v2, v8, v3, vcc
	v_lshlrev_b32_e32 v42, 2, v2
	v_mul_lo_u32 v2, v0, s5
	s_lshl_b32 s5, s61, 4
	s_add_i32 s5, s5, 0
	v_add_u32_e32 v2, s5, v2
	s_ashr_i32 s5, s4, 31
	s_lshl_b64 s[4:5], s[4:5], 11
	s_add_u32 s4, s10, s4
	s_addc_u32 s5, s11, s5
	s_add_u32 s4, s8, s4
	s_addc_u32 s5, s9, s5
	v_add_u32_e32 v43, 0x11000, v2
	v_lshl_add_u64 v[0:1], v[0:1], 1, s[4:5]
	s_mov_b32 s8, 0xf800000
	s_movk_i32 s9, 0x7fff
	s_brev_b32 s10, 64
	s_add_u32 s100, s6, 0x6000000
	s_addc_u32 s101, s7, 0
	v_lshl_add_u64 v[136:137], v[0:1], 0, s[100:101]
	global_load_ushort v120, v[136:137], off nt
	global_load_ushort v121, v[136:137], off offset:128 nt
	global_load_ushort v122, v[136:137], off offset:256 nt
	global_load_ushort v123, v[136:137], off offset:384 nt
	global_load_ushort v124, v[136:137], off offset:512 nt
	global_load_ushort v125, v[136:137], off offset:640 nt
	global_load_ushort v126, v[136:137], off offset:768 nt
	global_load_ushort v127, v[136:137], off offset:896 nt
	global_load_ushort v128, v[136:137], off offset:1024 nt
	global_load_ushort v129, v[136:137], off offset:1152 nt
	global_load_ushort v130, v[136:137], off offset:1280 nt
	global_load_ushort v131, v[136:137], off offset:1408 nt
	global_load_ushort v132, v[136:137], off offset:1536 nt
	global_load_ushort v133, v[136:137], off offset:1664 nt
	global_load_ushort v134, v[136:137], off offset:1792 nt
	global_load_ushort v135, v[136:137], off offset:1920 nt
	s_waitcnt vmcnt(0)
.LBB0_1026:
	v_lshl_add_u64 v[2:3], v[0:1], 0, s[6:7]
	v_add_u32_e32 v47, 0xfffef000, v43
	v_add_u32_e32 v48, 0xffff1200, v43
	v_add_u32_e32 v50, 0xffff5600, v43
	v_add_u32_e32 v51, 0xffff7800, v43
	v_add_u32_e32 v52, 0xffff9a00, v43
	v_add_u32_e32 v53, 0xffffbc00, v43
	v_add_u32_e32 v54, 0xffffde00, v43
	v_add_co_u32_e32 v46, vcc, 0x6000000, v2
	v_add_u32_e32 v49, 0xffff3400, v43
	ds_read_u16 v55, v43
	ds_read_u16 v56, v43 offset:8704
	ds_read_u16 v57, v43 offset:17408
	ds_read_u16 v58, v43 offset:26112
	ds_read_u16 v59, v43 offset:34816
	ds_read_u16 v60, v43 offset:43520
	ds_read_u16 v61, v43 offset:52224
	ds_read_u16 v62, v43 offset:60928
	ds_read_u16 v63, v47
	ds_read_u16 v64, v48
	ds_read_u16 v65, v49
	ds_read_u16 v50, v50
	ds_read_u16 v51, v51
	ds_read_u16 v52, v52
	ds_read_u16 v53, v53
	ds_read_u16 v54, v54
	v_add_co_u32_e64 v48, s[4:5], s10, v2
	v_addc_co_u32_e32 v47, vcc, 0, v3, vcc
	s_nop 0
	v_addc_co_u32_e64 v49, s[4:5], 0, v3, s[4:5]
	s_nop 0
	s_waitcnt lgkmcnt(14)
	v_lshlrev_b32_e32 v47, 16, v55
	v_lshlrev_b32_e32 v55, 16, v56
	s_waitcnt lgkmcnt(13)
	v_lshlrev_b32_e32 v56, 16, v57
	s_waitcnt lgkmcnt(12)
	v_lshlrev_b32_e32 v57, 16, v58
	s_waitcnt lgkmcnt(11)
	v_lshlrev_b32_e32 v58, 16, v59
	s_waitcnt lgkmcnt(10)
	v_lshlrev_b32_e32 v59, 16, v60
	s_waitcnt lgkmcnt(9)
	v_lshlrev_b32_e32 v60, 16, v61
	s_waitcnt lgkmcnt(8)
	v_lshlrev_b32_e32 v61, 16, v62
	s_waitcnt lgkmcnt(7)
	v_lshlrev_b32_e32 v62, 16, v63
	s_waitcnt lgkmcnt(6)
	v_lshlrev_b32_e32 v63, 16, v64
	s_waitcnt lgkmcnt(5)
	v_lshlrev_b32_e32 v64, 16, v65
	s_waitcnt lgkmcnt(4)
; #define LAS __attribute__((address_space(3)))
; __device__ __forceinline__ void peer_ln2_phase(LAS unsigned char* lds, int wave, int blk, const bf16* __restrict__ X1B, const bf16* __restrict__ YT, const float* __restrict__ g2, const float* __restrict__ b2, ...
;     ...
; #pragma unroll
;         for (int k = 0; k < 16; ++k) { const float xv = __uint_as_float((unsigned)__builtin_nontemporal_load((const unsigned short*)X1B + t * 1024 + lane + 64 * k) << 16); const unsigned yb = *(const LAS unsigned short*)(lds + (lane + 64 * k) * 136 + tk * 2);
;             z[k] = 1.41421356237309515f * xv + __uint_as_float(yb << 16); s += z[k]; }
; #pragma unroll
;         for (int o = 1; o < 64; o <<= 1) s += __shfl_xor(s, o);
;         const float mean = s * (1.0f / 1024.0f); float sq = 0.f;
; #pragma unroll
;         for (int k = 0; k < 16; ++k) { z[k] -= mean; sq += z[k] * z[k]; }
; #pragma unroll
;         for (int o = 1; o < 64; o <<= 1) sq += __shfl_xor(sq, o);
	v_lshlrev_b32_e32 v50, 16, v50
	s_waitcnt lgkmcnt(3)
	v_lshlrev_b32_e32 v51, 16, v51
	s_waitcnt lgkmcnt(2)
	v_lshlrev_b32_e32 v52, 16, v52
	s_waitcnt lgkmcnt(1)
	v_lshlrev_b32_e32 v53, 16, v53
	s_waitcnt lgkmcnt(0)
	v_lshlrev_b32_e32 v54, 16, v54
	s_add_u32 s6, s6, 0x800
	s_addc_u32 s7, s7, 0
	s_add_u32 s100, s6, 0x6000000
	s_addc_u32 s101, s7, 0
	v_add_u32_e32 v43, 2, v43
	s_cmpk_lg_i32 s6, 0x4000
	s_waitcnt vmcnt(31)
	v_lshlrev_b32_e32 v2, 16, v120
	s_waitcnt vmcnt(30)
	v_lshlrev_b32_e32 v3, 16, v121
	v_fmac_f32_e32 v62, 0x3fb504f3, v2
	s_waitcnt vmcnt(29)
	v_lshlrev_b32_e32 v65, 16, v122
	v_fmac_f32_e32 v63, 0x3fb504f3, v3
	v_add_f32_e32 v2, 0, v62
	s_waitcnt vmcnt(28)
	v_lshlrev_b32_e32 v66, 16, v123
	v_fmac_f32_e32 v64, 0x3fb504f3, v65
	v_add_f32_e32 v2, v2, v63
	s_waitcnt vmcnt(27)
	v_lshlrev_b32_e32 v67, 16, v124
	v_fmac_f32_e32 v50, 0x3fb504f3, v66
	v_add_f32_e32 v2, v2, v64
	s_waitcnt vmcnt(26)
	v_lshlrev_b32_e32 v68, 16, v125
	v_fmac_f32_e32 v51, 0x3fb504f3, v67
	v_add_f32_e32 v2, v2, v50
	s_waitcnt vmcnt(25)
	v_lshlrev_b32_e32 v69, 16, v126
	v_fmac_f32_e32 v52, 0x3fb504f3, v68
	v_add_f32_e32 v2, v2, v51
	s_waitcnt vmcnt(24)
	v_lshlrev_b32_e32 v70, 16, v127
	v_fmac_f32_e32 v53, 0x3fb504f3, v69
	v_add_f32_e32 v2, v2, v52
	s_waitcnt vmcnt(23)
	v_lshlrev_b32_e32 v71, 16, v128
	v_fmac_f32_e32 v54, 0x3fb504f3, v70
	v_add_f32_e32 v2, v2, v53
	s_waitcnt vmcnt(22)
	v_lshlrev_b32_e32 v72, 16, v129
	v_fmac_f32_e32 v47, 0x3fb504f3, v71
	v_add_f32_e32 v2, v2, v54
	s_waitcnt vmcnt(21)
	v_lshlrev_b32_e32 v73, 16, v130
	v_fmac_f32_e32 v55, 0x3fb504f3, v72
	v_add_f32_e32 v2, v2, v47
	s_waitcnt vmcnt(20)
	v_lshlrev_b32_e32 v74, 16, v131
	v_fmac_f32_e32 v56, 0x3fb504f3, v73
	v_add_f32_e32 v2, v2, v55
	s_waitcnt vmcnt(19)
	v_lshlrev_b32_e32 v75, 16, v132
	v_fmac_f32_e32 v57, 0x3fb504f3, v74
	v_add_f32_e32 v2, v2, v56
	s_waitcnt vmcnt(18)
	v_lshlrev_b32_e32 v76, 16, v133
	v_fmac_f32_e32 v58, 0x3fb504f3, v75
	v_add_f32_e32 v2, v2, v57
	s_waitcnt vmcnt(17)
	v_lshlrev_b32_e32 v77, 16, v134
	v_fmac_f32_e32 v59, 0x3fb504f3, v76
	v_add_f32_e32 v2, v2, v58
	s_waitcnt vmcnt(16)
	v_lshlrev_b32_e32 v46, 16, v135
	v_lshl_add_u64 v[136:137], v[0:1], 0, s[100:101]
	global_load_ushort v120, v[136:137], off nt
	global_load_ushort v121, v[136:137], off offset:128 nt
	global_load_ushort v122, v[136:137], off offset:256 nt
	global_load_ushort v123, v[136:137], off offset:384 nt
	global_load_ushort v124, v[136:137], off offset:512 nt
	global_load_ushort v125, v[136:137], off offset:640 nt
	global_load_ushort v126, v[136:137], off offset:768 nt
	global_load_ushort v127, v[136:137], off offset:896 nt
	global_load_ushort v128, v[136:137], off offset:1024 nt
	global_load_ushort v129, v[136:137], off offset:1152 nt
	global_load_ushort v130, v[136:137], off offset:1280 nt
	global_load_ushort v131, v[136:137], off offset:1408 nt
	global_load_ushort v132, v[136:137], off offset:1536 nt
	global_load_ushort v133, v[136:137], off offset:1664 nt
	global_load_ushort v134, v[136:137], off offset:1792 nt
	global_load_ushort v135, v[136:137], off offset:1920 nt
	v_fmac_f32_e32 v60, 0x3fb504f3, v77
	v_add_f32_e32 v2, v2, v59
	v_fmac_f32_e32 v61, 0x3fb504f3, v46
	v_add_f32_e32 v2, v2, v60
	v_add_f32_e32 v2, v2, v61
	s_nop 1
	v_add_f32_dpp v2, v2, v2 row_shr:1 row_mask:0xf bank_mask:0xf
	s_nop 1
	v_add_f32_dpp v2, v2, v2 row_shr:2 row_mask:0xf bank_mask:0xf
	s_nop 1
	v_add_f32_dpp v2, v2, v2 row_shr:4 row_mask:0xf bank_mask:0xf
	s_nop 1
	v_add_f32_dpp v2, v2, v2 row_shr:8 row_mask:0xf bank_mask:0xf
	s_nop 1
	v_add_f32_dpp v2, v2, v2 row_bcast:15 row_mask:0xa bank_mask:0xf
	s_nop 1
	v_add_f32_dpp v2, v2, v2 row_bcast:31 row_mask:0xc bank_mask:0xf
	s_nop 1
	v_readlane_b32 s98, v2, 63
	s_nop 1
	v_mov_b32_e32 v2, s98
	v_fmac_f32_e32 v63, 0xba800000, v2
	v_fmac_f32_e32 v62, 0xba800000, v2
	v_fmac_f32_e32 v64, 0xba800000, v2
	v_fmac_f32_e32 v50, 0xba800000, v2
	v_fmac_f32_e32 v51, 0xba800000, v2
	v_fmac_f32_e32 v52, 0xba800000, v2
	v_fmac_f32_e32 v53, 0xba800000, v2
	v_fmac_f32_e32 v54, 0xba800000, v2
	v_fmac_f32_e32 v47, 0xba800000, v2
	v_fmac_f32_e32 v55, 0xba800000, v2
	v_fmac_f32_e32 v56, 0xba800000, v2
	v_fmac_f32_e32 v57, 0xba800000, v2
	v_fmac_f32_e32 v58, 0xba800000, v2
	v_fmac_f32_e32 v59, 0xba800000, v2
	v_fmac_f32_e32 v60, 0xba800000, v2
	v_fmac_f32_e32 v61, 0xba800000, v2
	v_mul_f32_e32 v2, v63, v63
	v_fmac_f32_e32 v2, v62, v62
	v_fmac_f32_e32 v2, v64, v64
	v_fmac_f32_e32 v2, v50, v50
	v_fmac_f32_e32 v2, v51, v51
	v_fmac_f32_e32 v2, v52, v52
	v_fmac_f32_e32 v2, v53, v53
	v_fmac_f32_e32 v2, v54, v54
	v_fmac_f32_e32 v2, v47, v47
	v_fmac_f32_e32 v2, v55, v55
	v_fmac_f32_e32 v2, v56, v56
	v_fmac_f32_e32 v2, v57, v57
	v_fmac_f32_e32 v2, v58, v58
	v_fmac_f32_e32 v2, v59, v59
	v_fmac_f32_e32 v2, v60, v60
	v_fmac_f32_e32 v2, v61, v61
	s_nop 1
	v_add_f32_dpp v2, v2, v2 row_shr:1 row_mask:0xf bank_mask:0xf
	s_nop 1
	v_add_f32_dpp v2, v2, v2 row_shr:2 row_mask:0xf bank_mask:0xf
	s_nop 1
	v_add_f32_dpp v2, v2, v2 row_shr:4 row_mask:0xf bank_mask:0xf
	s_nop 1
	v_add_f32_dpp v2, v2, v2 row_shr:8 row_mask:0xf bank_mask:0xf
	s_nop 1
	v_add_f32_dpp v2, v2, v2 row_bcast:15 row_mask:0xa bank_mask:0xf
	s_nop 1
	v_add_f32_dpp v2, v2, v2 row_bcast:31 row_mask:0xc bank_mask:0xf
	s_nop 1
	v_readlane_b32 s98, v2, 63
	s_nop 1
	v_mov_b32_e32 v2, s98
	v_fmamk_f32 v2, v2, 0x3a800000, v44
	v_mul_f32_e32 v3, 0x4f800000, v2
	v_cmp_gt_f32_e32 vcc, s8, v2
; #define GAS __attribute__((address_space(1)))
; __device__ __forceinline__ unsigned f2bf(float f) { unsigned u = __builtin_bit_cast(unsigned, f); return (u + 0x7fffu + ((u >> 16) & 1u)) >> 16; }
; #define BOTH(k) (IN(k) && IN((k) + 1))
; __device__ __forceinline__ void peer_ln2_phase(LAS unsigned char* lds, int wave, int blk, const bf16* __restrict__ X1B, const bf16* __restrict__ YT, const float* __restrict__ g2, const float* __restrict__ b2, ...
;     ...
;         const float rstd = 1.0f / sqrtf(sq * (1.0f / 1024.0f) + 1e-5f);
; #pragma unroll
;         for (int k = 0; k < 16; ++k) { z[k] = z[k] * rstd * gv[k] + bv[k]; if (outf) __builtin_nontemporal_store(z[k], outf + t * 1024 + lane + 64 * k); }
;         if (outb) {
; #pragma unroll
;             for (int k = 0; k < 16; ++k) ((GAS unsigned short*)outb)[t * 1024 + lane + 64 * k] = (unsigned short)f2bf(z[k]); }
;     }
;     __syncthreads();
; template <int K> __device__ __forceinline__ void run_phase(Frame& F, const XcdBarrier& bar, int lo, int hi, unsigned char* lds) {
;     ...
;         if (BOTH(k)) {
;             constexpr bool LOCAL_SEAM = MK_LOCALBAR && (sub == 2 || (sub == 6 && l == 0));
;             bool local = false;
;             if (LOCAL_SEAM) local = __hip_atomic_load((unsigned*)(F.ctl + CW_LBAR + 24 * 64), __ATOMIC_RELAXED, __HIP_MEMORY_SCOPE_AGENT) == 0u;
;             constexpr bool PAIR_SEAM = MK_LOCALBAR && (sub == 0 || sub == 1);
;             bool pairok = false;
;             if (PAIR_SEAM) pairok = __hip_atomic_load((unsigned*)(F.ctl + CW_LBAR + 24 * 64), __ATOMIC_RELAXED, __HIP_MEMORY_SCOPE_AGENT) == 0u;
;             if (local) xcd_local_barrier((unsigned*)(F.ctl + CW_LBAR + ((sub == 2 ? l : 2) * 8 + (bx & 7)) * 64), (unsigned)(G >> 3), (unsigned*)(F.ctl + CW_BAR) + XB_TMO, F.wave);
;             else xcd_barrier(bar, F.wave, pairok ? ((bx & 7) >> 1) : -1);
	s_nop 1
	v_cndmask_b32_e32 v2, v2, v3, vcc
	v_sqrt_f32_e32 v3, v2
	s_nop 0
	v_add_u32_e32 v46, -1, v3
	v_add_u32_e32 v65, 1, v3
	v_fma_f32 v66, -v46, v3, v2
	v_fma_f32 v67, -v65, v3, v2
	v_cmp_ge_f32_e64 s[4:5], 0, v66
	s_nop 1
	v_cndmask_b32_e64 v3, v3, v46, s[4:5]
	v_cmp_lt_f32_e64 s[4:5], 0, v67
	s_nop 1
	v_cndmask_b32_e64 v3, v3, v65, s[4:5]
	v_mul_f32_e32 v46, 0x37800000, v3
	v_cndmask_b32_e32 v3, v3, v46, vcc
	v_cmp_class_f32_e32 vcc, v2, v45
	s_nop 1
	v_cndmask_b32_e32 v2, v3, v2, vcc
	v_div_scale_f32 v3, s[4:5], v2, v2, 1.0
	v_rcp_f32_e32 v65, v3
	v_div_scale_f32 v46, vcc, 1.0, v2, 1.0
	v_fma_f32 v66, -v3, v65, 1.0
	v_fmac_f32_e32 v65, v66, v65
	v_mul_f32_e32 v66, v46, v65
	v_fma_f32 v67, -v3, v66, v46
	v_fmac_f32_e32 v66, v67, v65
	v_fma_f32 v3, -v3, v66, v46
	v_div_fmas_f32 v3, v3, v65, v66
	v_div_fixup_f32 v2, v3, v2, 1.0
	v_mul_f32_e32 v3, v62, v2
	v_mul_f32_e32 v46, v63, v2
	v_mul_f32_e32 v62, v64, v2
	v_mul_f32_e32 v50, v50, v2
	v_mul_f32_e32 v51, v51, v2
	v_mul_f32_e32 v52, v52, v2
	v_mul_f32_e32 v53, v53, v2
	v_mul_f32_e32 v54, v54, v2
	v_mul_f32_e32 v47, v47, v2
	v_mul_f32_e32 v55, v55, v2
	v_mul_f32_e32 v56, v56, v2
	v_mul_f32_e32 v57, v57, v2
	v_mul_f32_e32 v58, v58, v2
	v_mul_f32_e32 v59, v59, v2
	v_mul_f32_e32 v60, v60, v2
	v_mul_f32_e32 v2, v61, v2
	v_fma_f32 v3, v4, v3, v13
	v_fma_f32 v46, v5, v46, v14
	v_fma_f32 v61, v6, v62, v15
	v_fma_f32 v50, v7, v50, v16
	v_fma_f32 v51, v9, v51, v17
	v_fma_f32 v52, v10, v52, v18
	v_fma_f32 v53, v11, v53, v19
	v_fma_f32 v54, v12, v54, v20
	v_fma_f32 v47, v21, v47, v29
	v_fma_f32 v55, v22, v55, v30
	v_fma_f32 v56, v23, v56, v31
	v_fma_f32 v57, v24, v57, v32
	v_fma_f32 v58, v25, v58, v33
	v_fma_f32 v59, v26, v59, v34
	v_fma_f32 v60, v27, v60, v35
	v_fma_f32 v2, v28, v2, v36
	v_bfe_u32 v62, v3, 16, 1
	v_bfe_u32 v63, v46, 16, 1
	v_bfe_u32 v64, v61, 16, 1
	v_bfe_u32 v65, v50, 16, 1
	v_bfe_u32 v66, v51, 16, 1
	v_bfe_u32 v67, v52, 16, 1
	v_bfe_u32 v68, v53, 16, 1
	v_bfe_u32 v69, v54, 16, 1
	v_bfe_u32 v70, v47, 16, 1
	v_bfe_u32 v71, v55, 16, 1
	v_bfe_u32 v72, v56, 16, 1
	v_bfe_u32 v73, v57, 16, 1
	v_bfe_u32 v74, v58, 16, 1
	v_bfe_u32 v75, v59, 16, 1
	v_bfe_u32 v76, v60, 16, 1
	v_bfe_u32 v77, v2, 16, 1
	v_add3_u32 v3, v3, v62, s9
	v_add3_u32 v46, v46, v63, s9
	v_add3_u32 v61, v61, v64, s9
	v_add3_u32 v50, v50, v65, s9
	v_add3_u32 v51, v51, v66, s9
	v_add3_u32 v52, v52, v67, s9
	v_add3_u32 v53, v53, v68, s9
	v_add3_u32 v54, v54, v69, s9
	v_add3_u32 v47, v47, v70, s9
	v_add3_u32 v55, v55, v71, s9
	v_add3_u32 v56, v56, v72, s9
	v_add3_u32 v57, v57, v73, s9
	v_add3_u32 v58, v58, v74, s9
	v_add3_u32 v59, v59, v75, s9
	v_add3_u32 v60, v60, v76, s9
	v_add3_u32 v2, v2, v77, s9
	global_store_short_d16_hi v[48:49], v3, off
	global_store_short_d16_hi v[48:49], v46, off offset:128
	global_store_short_d16_hi v[48:49], v61, off offset:256
	global_store_short_d16_hi v[48:49], v50, off offset:384
	global_store_short_d16_hi v[48:49], v51, off offset:512
	global_store_short_d16_hi v[48:49], v52, off offset:640
	global_store_short_d16_hi v[48:49], v53, off offset:768
	global_store_short_d16_hi v[48:49], v54, off offset:896
	global_store_short_d16_hi v[48:49], v47, off offset:1024
	global_store_short_d16_hi v[48:49], v55, off offset:1152
	global_store_short_d16_hi v[48:49], v56, off offset:1280
	global_store_short_d16_hi v[48:49], v57, off offset:1408
	global_store_short_d16_hi v[48:49], v58, off offset:1536
	global_store_short_d16_hi v[48:49], v59, off offset:1664
	global_store_short_d16_hi v[48:49], v60, off offset:1792
	global_store_short_d16_hi v[48:49], v2, off offset:1920
	s_cbranch_scc1 .LBB0_1026
	s_cmp_lt_u32 s41, 9
	s_barrier
	s_cbranch_scc1 .LBB0_1106
	v_mov_b32_e32 v0, 0x31000
	global_load_dword v0, v0, s[30:31] offset:2048 sc1
	s_waitcnt vmcnt(0)
	v_cmp_ne_u32_e32 vcc, 0, v0
	s_cbranch_vccz .LBB0_1041
	s_waitcnt vmcnt(0)
	s_andn2_b64 vcc, exec, s[38:39]
	s_barrier
	s_cbranch_vccnz .LBB0_1084
	v_mov_b32_e32 v0, v8
	s_nop 0
	v_cmp_eq_u32_e32 vcc, 0, v0
	s_and_saveexec_b64 s[4:5], vcc
	s_cbranch_execz .LBB0_1083
	s_add_i32 s6, 0, 0x27f60
	v_mov_b32_e32 v0, s6
	s_waitcnt vmcnt(0) expcnt(0) lgkmcnt(0)
	ds_read_b32 v2, v0
	s_add_i32 s6, 0, 0x27f64
	v_mov_b32_e32 v0, s6
	ds_read_b32 v0, v0
	s_waitcnt lgkmcnt(1)
	v_cmp_ne_u32_e32 vcc, 0, v2
	s_cbranch_vccnz .LBB0_1047
	v_readlane_b32 s6, v248, 0
	v_readlane_b32 s7, v248, 1
	s_load_dwordx2 s[10:11], s[6:7], 0x4
	s_add_u32 s6, s30, 0x4200
	s_addc_u32 s7, s31, 0
	s_add_u32 s8, s30, 0x4400
	s_addc_u32 s9, s31, 0
	s_waitcnt lgkmcnt(0)
	s_mul_i32 s59, s10, s60
	s_add_u32 s10, s30, 0x4500
	s_mul_i32 s59, s59, s11
	s_addc_u32 s11, s31, 0
	s_add_u32 s12, s30, 0x4600
	s_addc_u32 s13, s31, 0
	s_add_u32 s14, s30, 0x4700
	s_addc_u32 s15, s31, 0
	s_add_u32 s16, s30, 0x4800
	s_addc_u32 s17, s31, 0
	s_add_u32 s18, s30, 0x4900
	s_addc_u32 s19, s31, 0
	s_add_u32 s20, s30, 0x4a00
	s_addc_u32 s21, s31, 0
	s_add_u32 s22, s30, 0x4b00
	s_addc_u32 s23, s31, 0
	s_add_u32 s24, s30, 0x4c00
	s_addc_u32 s25, s31, 0
	s_add_u32 s26, s30, 0x4d00
	s_addc_u32 s27, s31, 0
	s_add_u32 s28, s30, 0x4e00
	s_addc_u32 s29, s31, 0
	s_add_u32 s42, s30, 0x4f00
	s_addc_u32 s43, s31, 0
	s_add_u32 s44, s30, 0x5000
	s_addc_u32 s45, s31, 0
	s_add_u32 s46, s30, 0x5100
	s_addc_u32 s47, s31, 0
	s_add_u32 s48, s30, 0x5200
	s_addc_u32 s49, s31, 0
	s_add_u32 s50, s30, 0x5300
	s_addc_u32 s51, s31, 0
	s_mov_b32 s62, 1
	v_mov_b32_e32 v17, 0
	s_branch .LBB0_1034
